# v9 + one-time stagger of the four row-panel sub-groups of each XCD ((wgid>>3)&3)*s_sleep36 at the G_out phase start; persists through the XCD-local chain so the sub-groups' store bursts do not coincid
# baseline (speedup 1.0000x reference)
.LBB0_1069:
	v_or_b32_e32 v1, s10, v139
	s_add_u32 s8, s8, 0x36300000
	v_lshlrev_b32_e32 v67, 6, v1
	s_movk_i32 s16, 0x3c0
	v_lshlrev_b32_e32 v68, 2, v1
	s_addc_u32 s9, s9, 0
	v_and_or_b32 v67, v67, s16, v66
	s_lshl_b32 s16, s28, 13
	v_and_b32_e32 v68, 32, v68
	v_bitop3_b32 v150, v67, s16, v68 bitop3:0xde
	v_lshlrev_b32_e32 v67, 2, v139
	v_lshl_or_b32 v66, v139, 6, v66
	s_lshl_b32 s16, s12, 12
	v_and_b32_e32 v67, 32, v67
	v_bitop3_b32 v146, v66, s16, v67 bitop3:0xde
	s_add_u32 s16, s50, 0x8000
	s_addc_u32 s17, s51, 0
	s_add_i32 m0, s20, 0x18000
	v_lshl_add_u64 v[66:67], s[16:17], 0, v[114:115]
	v_mov_b32_e32 v137, v115
	s_waitcnt vmcnt(2)
	s_barrier
	global_load_lds_dwordx4 v[66:67], off
	s_add_i32 m0, s20, 0x1a000
	v_lshl_add_u64 v[66:67], s[16:17], 0, v[136:137]
	s_add_u32 s16, s52, 0x8000
	v_mov_b32_e32 v133, v115
	s_addc_u32 s17, s53, 0
	s_add_i32 s59, s20, 0x8000
	v_mov_b32_e32 v135, v115
	global_load_lds_dwordx4 v[66:67], off
	v_lshl_add_u64 v[66:67], s[16:17], 0, v[132:133]
	s_mov_b32 m0, s59
	s_add_i32 s60, s20, 0xa000
	global_load_lds_dwordx4 v[66:67], off
	v_lshl_add_u64 v[66:67], s[16:17], 0, v[134:135]
	s_add_u32 s16, s50, 0x9000
	s_mov_b32 m0, s60
	s_addc_u32 s17, s51, 0
	global_load_lds_dwordx4 v[66:67], off
	s_add_i32 m0, s20, 0x1c000
	v_lshl_add_u64 v[66:67], s[16:17], 0, v[114:115]
	global_load_lds_dwordx4 v[66:67], off
	v_lshl_add_u64 v[66:67], s[16:17], 0, v[136:137]
	s_add_i32 m0, s20, 0x1e000
	v_lshlrev_b32_e32 v147, 3, v138
	global_load_lds_dwordx4 v[66:67], off
	s_waitcnt vmcnt(6)
	s_barrier
	s_waitcnt vmcnt(6)
	v_lshlrev_b32_e32 v116, 16, v62
	v_and_b32_e32 v117, 0xffff0000, v62
	v_lshlrev_b32_e32 v118, 16, v63
	v_and_b32_e32 v119, 0xffff0000, v63
	v_lshlrev_b32_e32 v124, 16, v64
	v_and_b32_e32 v125, 0xffff0000, v64
	v_lshlrev_b32_e32 v126, 16, v65
	v_and_b32_e32 v127, 0xffff0000, v65
	v_lshlrev_b32_e32 v120, 16, v58
	v_and_b32_e32 v121, 0xffff0000, v58
	v_lshlrev_b32_e32 v122, 16, v59
	v_and_b32_e32 v123, 0xffff0000, v59
	v_lshlrev_b32_e32 v128, 16, v60
	v_and_b32_e32 v129, 0xffff0000, v60
	v_lshlrev_b32_e32 v130, 16, v61
	v_and_b32_e32 v131, 0xffff0000, v61
	v_lshlrev_b32_e32 v98, 16, v54
	v_and_b32_e32 v99, 0xffff0000, v54
	v_lshlrev_b32_e32 v100, 16, v55
	v_and_b32_e32 v101, 0xffff0000, v55
	v_lshlrev_b32_e32 v102, 16, v56
	v_and_b32_e32 v103, 0xffff0000, v56
	v_lshlrev_b32_e32 v104, 16, v57
	v_and_b32_e32 v105, 0xffff0000, v57
	v_lshlrev_b32_e32 v106, 16, v50
	v_and_b32_e32 v107, 0xffff0000, v50
	v_lshlrev_b32_e32 v108, 16, v51
	v_and_b32_e32 v109, 0xffff0000, v51
	v_lshlrev_b32_e32 v110, 16, v52
	v_and_b32_e32 v111, 0xffff0000, v52
	v_lshlrev_b32_e32 v112, 16, v53
	v_and_b32_e32 v113, 0xffff0000, v53
	v_lshlrev_b32_e32 v82, 16, v46
	v_and_b32_e32 v83, 0xffff0000, v46
	v_lshlrev_b32_e32 v84, 16, v47
	v_and_b32_e32 v85, 0xffff0000, v47
	v_lshlrev_b32_e32 v90, 16, v48
	v_and_b32_e32 v91, 0xffff0000, v48
	v_lshlrev_b32_e32 v92, 16, v49
	v_and_b32_e32 v93, 0xffff0000, v49
	v_lshlrev_b32_e32 v86, 16, v42
	v_and_b32_e32 v87, 0xffff0000, v42
	v_lshlrev_b32_e32 v88, 16, v43
	v_and_b32_e32 v89, 0xffff0000, v43
	v_lshlrev_b32_e32 v94, 16, v44
	v_and_b32_e32 v95, 0xffff0000, v44
	v_lshlrev_b32_e32 v96, 16, v45
	v_and_b32_e32 v97, 0xffff0000, v45
	v_lshlrev_b32_e32 v58, 16, v38
	v_and_b32_e32 v59, 0xffff0000, v38
	v_lshlrev_b32_e32 v60, 16, v39
	v_and_b32_e32 v61, 0xffff0000, v39
	v_lshlrev_b32_e32 v70, 16, v40
	v_and_b32_e32 v71, 0xffff0000, v40
	v_lshlrev_b32_e32 v72, 16, v41
	v_and_b32_e32 v73, 0xffff0000, v41
	v_lshlrev_b32_e32 v74, 16, v30
	v_and_b32_e32 v75, 0xffff0000, v30
	v_lshlrev_b32_e32 v76, 16, v31
	v_and_b32_e32 v77, 0xffff0000, v31
	v_lshlrev_b32_e32 v78, 16, v32
	v_and_b32_e32 v79, 0xffff0000, v32
	v_lshlrev_b32_e32 v80, 16, v33
	v_and_b32_e32 v81, 0xffff0000, v33
	v_lshlrev_b32_e32 v50, 16, v34
	v_and_b32_e32 v51, 0xffff0000, v34
	v_lshlrev_b32_e32 v52, 16, v35
	v_and_b32_e32 v53, 0xffff0000, v35
	v_lshlrev_b32_e32 v62, 16, v36
	v_and_b32_e32 v63, 0xffff0000, v36
	v_lshlrev_b32_e32 v64, 16, v37
	v_and_b32_e32 v65, 0xffff0000, v37
	v_lshlrev_b32_e32 v54, 16, v26
	v_and_b32_e32 v55, 0xffff0000, v26
	v_lshlrev_b32_e32 v56, 16, v27
	v_and_b32_e32 v57, 0xffff0000, v27
	v_lshlrev_b32_e32 v66, 16, v28
	v_and_b32_e32 v67, 0xffff0000, v28
	v_lshlrev_b32_e32 v68, 16, v29
	v_and_b32_e32 v69, 0xffff0000, v29
	v_lshlrev_b32_e32 v34, 16, v22
	v_and_b32_e32 v35, 0xffff0000, v22
	v_lshlrev_b32_e32 v36, 16, v23
	v_and_b32_e32 v37, 0xffff0000, v23
	v_lshlrev_b32_e32 v38, 16, v24
	v_and_b32_e32 v39, 0xffff0000, v24
	v_lshlrev_b32_e32 v40, 16, v25
	v_and_b32_e32 v41, 0xffff0000, v25
	v_lshlrev_b32_e32 v42, 16, v18
	v_and_b32_e32 v43, 0xffff0000, v18
	v_lshlrev_b32_e32 v44, 16, v19
	v_and_b32_e32 v45, 0xffff0000, v19
	v_lshlrev_b32_e32 v46, 16, v20
	v_and_b32_e32 v47, 0xffff0000, v20
	v_lshlrev_b32_e32 v48, 16, v21
	v_and_b32_e32 v49, 0xffff0000, v21
	v_lshlrev_b32_e32 v18, 16, v10
	v_and_b32_e32 v19, 0xffff0000, v10
	v_lshlrev_b32_e32 v20, 16, v11
	v_and_b32_e32 v21, 0xffff0000, v11
	v_lshlrev_b32_e32 v26, 16, v12
	v_and_b32_e32 v27, 0xffff0000, v12
	v_lshlrev_b32_e32 v28, 16, v13
	v_and_b32_e32 v29, 0xffff0000, v13
	v_lshlrev_b32_e32 v22, 16, v2
	v_and_b32_e32 v23, 0xffff0000, v2
	v_lshlrev_b32_e32 v24, 16, v3
	v_and_b32_e32 v25, 0xffff0000, v3
	v_lshlrev_b32_e32 v30, 16, v4
	v_and_b32_e32 v31, 0xffff0000, v4
	v_lshlrev_b32_e32 v32, 16, v5
	v_and_b32_e32 v33, 0xffff0000, v5
	v_lshlrev_b32_e32 v2, 16, v6
	v_and_b32_e32 v3, 0xffff0000, v6
	v_lshlrev_b32_e32 v4, 16, v7
	v_and_b32_e32 v5, 0xffff0000, v7
	v_lshlrev_b32_e32 v6, 16, v8
	v_and_b32_e32 v7, 0xffff0000, v8
	v_lshlrev_b32_e32 v8, 16, v9
	v_and_b32_e32 v9, 0xffff0000, v9
	v_lshlrev_b32_e32 v10, 16, v14
	v_and_b32_e32 v11, 0xffff0000, v14
	v_lshlrev_b32_e32 v12, 16, v15
	v_and_b32_e32 v13, 0xffff0000, v15
	v_lshlrev_b32_e32 v14, 16, v16
	v_and_b32_e32 v15, 0xffff0000, v16
	v_lshlrev_b32_e32 v16, 16, v17
	v_and_b32_e32 v17, 0xffff0000, v17
	v_mov_b32_e32 v149, s11
	v_or_b32_e32 v148, s10, v139
	v_cmp_eq_u32_e64 s[38:39], 0, v138
	v_lshlrev_b64 v[138:139], 7, v[148:149]
	v_lshlrev_b32_e32 v148, 1, v147
	v_lshlrev_b32_e32 v147, 10, v140
	v_and_b32_e32 v147, 0xfffff800, v147
	v_lshl_add_u32 v141, v141, 7, v147
	v_and_b32_e32 v140, 1, v140
	v_lshl_or_b32 v140, v140, 6, v141
	v_lshl_add_u32 v140, v142, 1, v140
	v_lshlrev_b32_e32 v142, 10, v143
	v_and_b32_e32 v142, 0xfffff800, v142
	v_lshl_add_u32 v142, v144, 7, v142
	v_and_b32_e32 v143, 1, v143
	s_cmpk_lt_u32 s24, 0x100
	v_lshl_add_u64 v[138:139], s[26:27], 0, v[138:139]
	v_mov_b32_e32 v149, v115
	v_lshl_or_b32 v142, v143, 6, v142
	s_cselect_b64 s[10:11], -1, 0
	s_mov_b32 s61, 0
	s_ashr_i32 s62, s7, 31
	v_lshl_add_u64 v[138:139], v[138:139], 0, v[148:149]
	v_mov_b32_e32 v141, v115
	v_lshl_add_u32 v142, v145, 1, v142
	v_mov_b32_e32 v143, v115
	v_add_u32_e32 v147, 0, v150
	v_readlane_b32 s100, v254, 0
	s_nop 3
	s_bfe_u32 s100, s100, 0x20003
	s_cmp_eq_u32 s100, 0
	s_cbranch_scc1 .Lstg_done_x
.Lstg_loop_x:
	s_sleep 36
	s_sub_u32 s100, s100, 1
	s_cmp_lg_u32 s100, 0
	s_cbranch_scc1 .Lstg_loop_x
.Lstg_done_x:
	s_branch .LBB0_1072
.LBB0_1070:
	s_waitcnt vmcnt(0)
	v_lshlrev_b32_e32 v116, 16, v62
	v_and_b32_e32 v117, 0xffff0000, v62
	v_lshlrev_b32_e32 v118, 16, v63
	v_and_b32_e32 v119, 0xffff0000, v63
	v_lshlrev_b32_e32 v124, 16, v64
	v_and_b32_e32 v125, 0xffff0000, v64
	v_lshlrev_b32_e32 v126, 16, v65
	v_and_b32_e32 v127, 0xffff0000, v65
	v_lshlrev_b32_e32 v120, 16, v58
	v_and_b32_e32 v121, 0xffff0000, v58
	v_lshlrev_b32_e32 v122, 16, v59
	v_and_b32_e32 v123, 0xffff0000, v59
	v_lshlrev_b32_e32 v128, 16, v60
	v_and_b32_e32 v129, 0xffff0000, v60
	v_lshlrev_b32_e32 v130, 16, v61
	v_and_b32_e32 v131, 0xffff0000, v61
	v_lshlrev_b32_e32 v98, 16, v54
	v_and_b32_e32 v99, 0xffff0000, v54
	v_lshlrev_b32_e32 v100, 16, v55
	v_and_b32_e32 v101, 0xffff0000, v55
	v_lshlrev_b32_e32 v102, 16, v56
	v_and_b32_e32 v103, 0xffff0000, v56
	v_lshlrev_b32_e32 v104, 16, v57
	v_and_b32_e32 v105, 0xffff0000, v57
	v_lshlrev_b32_e32 v106, 16, v50
	v_and_b32_e32 v107, 0xffff0000, v50
	v_lshlrev_b32_e32 v108, 16, v51
	v_and_b32_e32 v109, 0xffff0000, v51
	v_lshlrev_b32_e32 v110, 16, v52
	v_and_b32_e32 v111, 0xffff0000, v52
	v_lshlrev_b32_e32 v112, 16, v53
	v_and_b32_e32 v113, 0xffff0000, v53
	v_lshlrev_b32_e32 v82, 16, v46
	v_and_b32_e32 v83, 0xffff0000, v46
	v_lshlrev_b32_e32 v84, 16, v47
	v_and_b32_e32 v85, 0xffff0000, v47
	v_lshlrev_b32_e32 v90, 16, v48
	v_and_b32_e32 v91, 0xffff0000, v48
	v_lshlrev_b32_e32 v92, 16, v49
	v_and_b32_e32 v93, 0xffff0000, v49
	v_lshlrev_b32_e32 v86, 16, v42
	v_and_b32_e32 v87, 0xffff0000, v42
	v_lshlrev_b32_e32 v88, 16, v43
	v_and_b32_e32 v89, 0xffff0000, v43
	v_lshlrev_b32_e32 v94, 16, v44
	v_and_b32_e32 v95, 0xffff0000, v44
	v_lshlrev_b32_e32 v96, 16, v45
	v_and_b32_e32 v97, 0xffff0000, v45
	v_lshlrev_b32_e32 v58, 16, v38
	v_and_b32_e32 v59, 0xffff0000, v38
	v_lshlrev_b32_e32 v60, 16, v39
	v_and_b32_e32 v61, 0xffff0000, v39
	v_lshlrev_b32_e32 v70, 16, v40
	v_and_b32_e32 v71, 0xffff0000, v40
	v_lshlrev_b32_e32 v72, 16, v41
	v_and_b32_e32 v73, 0xffff0000, v41
	v_lshlrev_b32_e32 v74, 16, v34
	v_and_b32_e32 v75, 0xffff0000, v34
	v_lshlrev_b32_e32 v76, 16, v35
	v_and_b32_e32 v77, 0xffff0000, v35
	v_lshlrev_b32_e32 v78, 16, v36
	v_and_b32_e32 v79, 0xffff0000, v36
	v_lshlrev_b32_e32 v80, 16, v37
	v_and_b32_e32 v81, 0xffff0000, v37
	v_lshlrev_b32_e32 v50, 16, v30
	v_and_b32_e32 v51, 0xffff0000, v30
	v_lshlrev_b32_e32 v52, 16, v31
	v_and_b32_e32 v53, 0xffff0000, v31
	v_lshlrev_b32_e32 v62, 16, v32
	v_and_b32_e32 v63, 0xffff0000, v32
	v_lshlrev_b32_e32 v64, 16, v33
	v_and_b32_e32 v65, 0xffff0000, v33
	v_lshlrev_b32_e32 v54, 16, v26
	v_and_b32_e32 v55, 0xffff0000, v26
	v_lshlrev_b32_e32 v56, 16, v27
	v_and_b32_e32 v57, 0xffff0000, v27
	v_lshlrev_b32_e32 v66, 16, v28
	v_and_b32_e32 v67, 0xffff0000, v28
	v_lshlrev_b32_e32 v68, 16, v29
	v_and_b32_e32 v69, 0xffff0000, v29
	v_lshlrev_b32_e32 v34, 16, v22
	v_and_b32_e32 v35, 0xffff0000, v22
	v_lshlrev_b32_e32 v36, 16, v23
	v_and_b32_e32 v37, 0xffff0000, v23
	v_lshlrev_b32_e32 v38, 16, v24
	v_and_b32_e32 v39, 0xffff0000, v24
	v_lshlrev_b32_e32 v40, 16, v25
	v_and_b32_e32 v41, 0xffff0000, v25
	v_lshlrev_b32_e32 v42, 16, v18
	v_and_b32_e32 v43, 0xffff0000, v18
	v_lshlrev_b32_e32 v44, 16, v19
	v_and_b32_e32 v45, 0xffff0000, v19
	v_lshlrev_b32_e32 v46, 16, v20
	v_and_b32_e32 v47, 0xffff0000, v20
	v_lshlrev_b32_e32 v48, 16, v21
	v_and_b32_e32 v49, 0xffff0000, v21
	v_lshlrev_b32_e32 v18, 16, v10
	v_and_b32_e32 v19, 0xffff0000, v10
	v_lshlrev_b32_e32 v20, 16, v11
	v_and_b32_e32 v21, 0xffff0000, v11
	v_lshlrev_b32_e32 v26, 16, v12
	v_and_b32_e32 v27, 0xffff0000, v12
	v_lshlrev_b32_e32 v28, 16, v13
	v_and_b32_e32 v29, 0xffff0000, v13
	v_lshlrev_b32_e32 v22, 16, v2
	v_and_b32_e32 v23, 0xffff0000, v2
	v_lshlrev_b32_e32 v24, 16, v3
	v_and_b32_e32 v25, 0xffff0000, v3
	v_lshlrev_b32_e32 v30, 16, v4
	v_and_b32_e32 v31, 0xffff0000, v4
	v_lshlrev_b32_e32 v32, 16, v5
	v_and_b32_e32 v33, 0xffff0000, v5
	v_lshlrev_b32_e32 v2, 16, v6
	v_and_b32_e32 v3, 0xffff0000, v6
	v_lshlrev_b32_e32 v4, 16, v7
	v_and_b32_e32 v5, 0xffff0000, v7
	v_lshlrev_b32_e32 v6, 16, v8
	v_and_b32_e32 v7, 0xffff0000, v8
	v_lshlrev_b32_e32 v8, 16, v9
	v_and_b32_e32 v9, 0xffff0000, v9
	v_lshlrev_b32_e32 v10, 16, v14
	v_and_b32_e32 v11, 0xffff0000, v14
	v_lshlrev_b32_e32 v12, 16, v15
	v_and_b32_e32 v13, 0xffff0000, v15
	v_lshlrev_b32_e32 v14, 16, v16
	v_and_b32_e32 v15, 0xffff0000, v16
	v_lshlrev_b32_e32 v16, 16, v17
	v_and_b32_e32 v17, 0xffff0000, v17
	s_mov_b64 s[40:41], 0
